# stack12 + grid-barrier poll loops back off s_sleep 4 instead of s_sleep 1 between polls (less polling traffic on the barrier flags)
# speedup vs baseline: 1.0043x; 1.0041x over previous
.LBB0_101:
	global_load_dword v16, v17, s[6:7] sc1
	global_load_dword v1, v17, s[8:9] sc1
	global_load_dword v2, v17, s[10:11] sc1
	global_load_dword v3, v17, s[12:13] sc1
	global_load_dword v4, v17, s[14:15] sc1
	global_load_dword v5, v17, s[16:17] sc1
	global_load_dword v6, v17, s[18:19] sc1
	global_load_dword v7, v17, s[20:21] sc1
	global_load_dword v8, v17, s[22:23] sc1
	global_load_dword v9, v17, s[24:25] sc1
	global_load_dword v10, v17, s[26:27] sc1
	global_load_dword v11, v17, s[28:29] sc1
	global_load_dword v12, v17, s[30:31] sc1
	global_load_dword v13, v17, s[34:35] sc1
	global_load_dword v14, v17, s[36:37] sc1
	global_load_dword v15, v17, s[38:39] sc1
	s_mov_b64 s[40:41], -1
	s_mov_b64 s[42:43], -1
	s_waitcnt vmcnt(14)
	v_add_u32_e32 v18, v1, v16
	s_waitcnt vmcnt(13)
	v_add_u32_e32 v18, v18, v2
	s_waitcnt vmcnt(12)
	v_add_u32_e32 v18, v18, v3
	s_waitcnt vmcnt(11)
	v_add_u32_e32 v18, v18, v4
	s_waitcnt vmcnt(10)
	v_add_u32_e32 v18, v18, v5
	s_waitcnt vmcnt(9)
	v_add_u32_e32 v18, v18, v6
	s_waitcnt vmcnt(8)
	v_add_u32_e32 v18, v18, v7
	s_waitcnt vmcnt(7)
	v_add_u32_e32 v18, v18, v8
	s_waitcnt vmcnt(6)
	v_add_u32_e32 v18, v18, v9
	s_waitcnt vmcnt(5)
	v_add_u32_e32 v18, v18, v10
	s_waitcnt vmcnt(4)
	v_add_u32_e32 v18, v18, v11
	s_waitcnt vmcnt(3)
	v_add_u32_e32 v18, v18, v12
	s_waitcnt vmcnt(2)
	v_add_u32_e32 v18, v18, v13
	s_waitcnt vmcnt(1)
	v_add_u32_e32 v18, v18, v14
	s_waitcnt vmcnt(0)
	v_add_u32_e32 v18, v18, v15
	v_cmp_eq_u32_e32 vcc, s33, v18
	s_cbranch_vccnz .LBB0_100
	s_and_b32 s40, s47, 0xff
	s_cmp_eq_u32 s40, 0
	s_mov_b64 s[40:41], -1
	s_mov_b64 s[44:45], -1
	s_sleep 4
	s_cbranch_scc0 .LBB0_105
	global_load_dword v18, v17, s[4:5] sc1
	s_waitcnt vmcnt(0)
	v_cmp_eq_u32_e32 vcc, 0, v18
	s_cbranch_vccnz .LBB0_107
	s_mov_b64 s[44:45], 0

.LBB0_119:
	s_and_b32 s20, s24, 0xff
	s_mov_b64 s[18:19], -1
	s_cmp_lg_u32 s20, 0
	s_mov_b64 s[22:23], -1
	s_sleep 4
	s_cbranch_scc1 .LBB0_122
	global_load_dword v3, v1, s[10:11] sc1
	s_waitcnt vmcnt(0)
	v_cmp_eq_u32_e32 vcc, 0, v3
	s_cbranch_vccnz .LBB0_124
	s_mov_b64 s[22:23], 0
	s_mov_b64 s[20:21], -1

.LBB0_136:
	s_and_b32 s18, s24, 0xff
	s_cmp_lg_u32 s18, 0
	s_mov_b64 s[20:21], -1
	s_sleep 4
	s_cbranch_scc1 .LBB0_139
	global_load_dword v2, v1, s[10:11] sc1
	s_waitcnt vmcnt(0)
	v_cmp_eq_u32_e32 vcc, 0, v2
	s_cbranch_vccnz .LBB0_141
	s_mov_b64 s[20:21], 0
	s_mov_b64 s[18:19], -1

.LBB0_533:
	global_load_dword v16, v17, s[6:7] sc1
	global_load_dword v1, v17, s[8:9] sc1
	global_load_dword v2, v17, s[10:11] sc1
	global_load_dword v3, v17, s[12:13] sc1
	global_load_dword v4, v17, s[14:15] sc1
	global_load_dword v5, v17, s[16:17] sc1
	global_load_dword v6, v17, s[18:19] sc1
	global_load_dword v7, v17, s[20:21] sc1
	global_load_dword v8, v17, s[22:23] sc1
	global_load_dword v9, v17, s[24:25] sc1
	global_load_dword v10, v17, s[26:27] sc1
	global_load_dword v11, v17, s[28:29] sc1
	global_load_dword v12, v17, s[30:31] sc1
	global_load_dword v13, v17, s[34:35] sc1
	global_load_dword v14, v17, s[36:37] sc1
	global_load_dword v15, v17, s[38:39] sc1
	s_mov_b64 s[40:41], -1
	s_mov_b64 s[42:43], -1
	s_waitcnt vmcnt(14)
	v_add_u32_e32 v18, v1, v16
	s_waitcnt vmcnt(13)
	v_add_u32_e32 v18, v18, v2
	s_waitcnt vmcnt(12)
	v_add_u32_e32 v18, v18, v3
	s_waitcnt vmcnt(11)
	v_add_u32_e32 v18, v18, v4
	s_waitcnt vmcnt(10)
	v_add_u32_e32 v18, v18, v5
	s_waitcnt vmcnt(9)
	v_add_u32_e32 v18, v18, v6
	s_waitcnt vmcnt(8)
	v_add_u32_e32 v18, v18, v7
	s_waitcnt vmcnt(7)
	v_add_u32_e32 v18, v18, v8
	s_waitcnt vmcnt(6)
	v_add_u32_e32 v18, v18, v9
	s_waitcnt vmcnt(5)
	v_add_u32_e32 v18, v18, v10
	s_waitcnt vmcnt(4)
	v_add_u32_e32 v18, v18, v11
	s_waitcnt vmcnt(3)
	v_add_u32_e32 v18, v18, v12
	s_waitcnt vmcnt(2)
	v_add_u32_e32 v18, v18, v13
	s_waitcnt vmcnt(1)
	v_add_u32_e32 v18, v18, v14
	s_waitcnt vmcnt(0)
	v_add_u32_e32 v18, v18, v15
	v_cmp_eq_u32_e32 vcc, s33, v18
	s_cbranch_vccnz .LBB0_532
	s_and_b32 s40, s46, 0xff
	s_cmp_eq_u32 s40, 0
	s_mov_b64 s[40:41], -1
	s_mov_b64 s[44:45], -1
	s_sleep 4
	s_cbranch_scc0 .LBB0_537
	global_load_dword v18, v17, s[4:5] sc1
	s_waitcnt vmcnt(0)
	v_cmp_eq_u32_e32 vcc, 0, v18
	s_cbranch_vccnz .LBB0_539
	s_mov_b64 s[44:45], 0

.LBB0_1358:
	global_load_dword v16, v17, s[8:9] sc1
	global_load_dword v1, v17, s[10:11] sc1
	global_load_dword v2, v17, s[12:13] sc1
	global_load_dword v3, v17, s[14:15] sc1
	global_load_dword v4, v17, s[16:17] sc1
	global_load_dword v5, v17, s[18:19] sc1
	global_load_dword v6, v17, s[20:21] sc1
	global_load_dword v7, v17, s[22:23] sc1
	global_load_dword v8, v17, s[24:25] sc1
	global_load_dword v9, v17, s[26:27] sc1
	global_load_dword v10, v17, s[28:29] sc1
	global_load_dword v11, v17, s[30:31] sc1
	global_load_dword v12, v17, s[34:35] sc1
	global_load_dword v13, v17, s[36:37] sc1
	global_load_dword v14, v17, s[38:39] sc1
	global_load_dword v15, v17, s[40:41] sc1
	s_mov_b64 s[42:43], -1
	s_mov_b64 s[44:45], -1
	s_waitcnt vmcnt(14)
	v_add_u32_e32 v18, v1, v16
	s_waitcnt vmcnt(13)
	v_add_u32_e32 v18, v18, v2
	s_waitcnt vmcnt(12)
	v_add_u32_e32 v18, v18, v3
	s_waitcnt vmcnt(11)
	v_add_u32_e32 v18, v18, v4
	s_waitcnt vmcnt(10)
	v_add_u32_e32 v18, v18, v5
	s_waitcnt vmcnt(9)
	v_add_u32_e32 v18, v18, v6
	s_waitcnt vmcnt(8)
	v_add_u32_e32 v18, v18, v7
	s_waitcnt vmcnt(7)
	v_add_u32_e32 v18, v18, v8
	s_waitcnt vmcnt(6)
	v_add_u32_e32 v18, v18, v9
	s_waitcnt vmcnt(5)
	v_add_u32_e32 v18, v18, v10
	s_waitcnt vmcnt(4)
	v_add_u32_e32 v18, v18, v11
	s_waitcnt vmcnt(3)
	v_add_u32_e32 v18, v18, v12
	s_waitcnt vmcnt(2)
	v_add_u32_e32 v18, v18, v13
	s_waitcnt vmcnt(1)
	v_add_u32_e32 v18, v18, v14
	s_waitcnt vmcnt(0)
	v_add_u32_e32 v18, v18, v15
	v_cmp_eq_u32_e32 vcc, s33, v18
	s_cbranch_vccnz .LBB0_1357
	s_and_b32 s42, s48, 0xff
	s_cmp_eq_u32 s42, 0
	s_mov_b64 s[42:43], -1
	s_mov_b64 s[46:47], -1
	s_sleep 4
	s_cbranch_scc0 .LBB0_1362
	global_load_dword v18, v17, s[6:7] sc1
	s_waitcnt vmcnt(0)
	v_cmp_eq_u32_e32 vcc, 0, v18
	s_cbranch_vccnz .LBB0_1364
	s_mov_b64 s[46:47], 0

.LBB0_1376:
	s_and_b32 s22, s26, 0xff
	s_mov_b64 s[20:21], -1
	s_cmp_lg_u32 s22, 0
	s_mov_b64 s[24:25], -1
	s_sleep 4
	s_cbranch_scc1 .LBB0_1379
	global_load_dword v3, v1, s[12:13] sc1
	s_waitcnt vmcnt(0)
	v_cmp_eq_u32_e32 vcc, 0, v3
	s_cbranch_vccnz .LBB0_1381
	s_mov_b64 s[24:25], 0
	s_mov_b64 s[22:23], -1

.LBB0_1393:
	s_and_b32 s20, s26, 0xff
	s_cmp_lg_u32 s20, 0
	s_mov_b64 s[22:23], -1
	s_sleep 4
	s_cbranch_scc1 .LBB0_1396
	global_load_dword v2, v1, s[12:13] sc1
	s_waitcnt vmcnt(0)
	v_cmp_eq_u32_e32 vcc, 0, v2
	s_cbranch_vccnz .LBB0_1398
	s_mov_b64 s[22:23], 0
	s_mov_b64 s[20:21], -1

.LBB0_1491:
	global_load_dword v16, v17, s[8:9] sc1
	global_load_dword v1, v17, s[10:11] sc1
	global_load_dword v2, v17, s[12:13] sc1
	global_load_dword v3, v17, s[14:15] sc1
	global_load_dword v4, v17, s[16:17] sc1
	global_load_dword v5, v17, s[18:19] sc1
	global_load_dword v6, v17, s[22:23] sc1
	global_load_dword v7, v17, s[24:25] sc1
	global_load_dword v8, v17, s[26:27] sc1
	global_load_dword v9, v17, s[28:29] sc1
	global_load_dword v10, v17, s[30:31] sc1
	global_load_dword v11, v17, s[34:35] sc1
	global_load_dword v12, v17, s[36:37] sc1
	global_load_dword v13, v17, s[38:39] sc1
	global_load_dword v14, v17, s[40:41] sc1
	global_load_dword v15, v17, s[42:43] sc1
	s_mov_b64 s[44:45], -1
	s_mov_b64 s[46:47], -1
	s_waitcnt vmcnt(14)
	v_add_u32_e32 v18, v1, v16
	s_waitcnt vmcnt(13)
	v_add_u32_e32 v18, v18, v2
	s_waitcnt vmcnt(12)
	v_add_u32_e32 v18, v18, v3
	s_waitcnt vmcnt(11)
	v_add_u32_e32 v18, v18, v4
	s_waitcnt vmcnt(10)
	v_add_u32_e32 v18, v18, v5
	s_waitcnt vmcnt(9)
	v_add_u32_e32 v18, v18, v6
	s_waitcnt vmcnt(8)
	v_add_u32_e32 v18, v18, v7
	s_waitcnt vmcnt(7)
	v_add_u32_e32 v18, v18, v8
	s_waitcnt vmcnt(6)
	v_add_u32_e32 v18, v18, v9
	s_waitcnt vmcnt(5)
	v_add_u32_e32 v18, v18, v10
	s_waitcnt vmcnt(4)
	v_add_u32_e32 v18, v18, v11
	s_waitcnt vmcnt(3)
	v_add_u32_e32 v18, v18, v12
	s_waitcnt vmcnt(2)
	v_add_u32_e32 v18, v18, v13
	s_waitcnt vmcnt(1)
	v_add_u32_e32 v18, v18, v14
	s_waitcnt vmcnt(0)
	v_add_u32_e32 v18, v18, v15
	v_cmp_eq_u32_e32 vcc, s33, v18
	s_cbranch_vccnz .LBB0_1490
	s_and_b32 s44, s50, 0xff
	s_cmp_eq_u32 s44, 0
	s_mov_b64 s[44:45], -1
	s_mov_b64 s[48:49], -1
	s_sleep 4
	s_cbranch_scc0 .LBB0_1495
	global_load_dword v18, v17, s[6:7] sc1
	s_waitcnt vmcnt(0)
	v_cmp_eq_u32_e32 vcc, 0, v18
	s_cbranch_vccnz .LBB0_1497
	s_mov_b64 s[48:49], 0

.LBB0_1509:
	s_and_b32 s24, s28, 0xff
	s_mov_b64 s[22:23], -1
	s_cmp_lg_u32 s24, 0
	s_mov_b64 s[26:27], -1
	s_sleep 4
	s_cbranch_scc1 .LBB0_1512
	global_load_dword v3, v1, s[12:13] sc1
	s_waitcnt vmcnt(0)
	v_cmp_eq_u32_e32 vcc, 0, v3
	s_cbranch_vccnz .LBB0_1514
	s_mov_b64 s[26:27], 0
	s_mov_b64 s[24:25], -1

.LBB0_1526:
	s_and_b32 s22, s28, 0xff
	s_cmp_lg_u32 s22, 0
	s_mov_b64 s[24:25], -1
	s_sleep 4
	s_cbranch_scc1 .LBB0_1529
	global_load_dword v2, v1, s[12:13] sc1
	s_waitcnt vmcnt(0)
	v_cmp_eq_u32_e32 vcc, 0, v2
	s_cbranch_vccnz .LBB0_1531
	s_mov_b64 s[24:25], 0
	s_mov_b64 s[22:23], -1

.LBB0_2204:
	global_load_dword v16, v17, s[6:7] sc1
	global_load_dword v1, v17, s[8:9] sc1
	global_load_dword v2, v17, s[10:11] sc1
	global_load_dword v3, v17, s[12:13] sc1
	global_load_dword v4, v17, s[14:15] sc1
	global_load_dword v5, v17, s[16:17] sc1
	global_load_dword v6, v17, s[18:19] sc1
	global_load_dword v7, v17, s[22:23] sc1
	global_load_dword v8, v17, s[24:25] sc1
	global_load_dword v9, v17, s[26:27] sc1
	global_load_dword v10, v17, s[28:29] sc1
	global_load_dword v11, v17, s[30:31] sc1
	global_load_dword v12, v17, s[34:35] sc1
	global_load_dword v13, v17, s[36:37] sc1
	global_load_dword v14, v17, s[38:39] sc1
	global_load_dword v15, v17, s[40:41] sc1
	s_mov_b64 s[42:43], -1
	s_mov_b64 s[44:45], -1
	s_waitcnt vmcnt(14)
	v_add_u32_e32 v18, v1, v16
	s_waitcnt vmcnt(13)
	v_add_u32_e32 v18, v18, v2
	s_waitcnt vmcnt(12)
	v_add_u32_e32 v18, v18, v3
	s_waitcnt vmcnt(11)
	v_add_u32_e32 v18, v18, v4
	s_waitcnt vmcnt(10)
	v_add_u32_e32 v18, v18, v5
	s_waitcnt vmcnt(9)
	v_add_u32_e32 v18, v18, v6
	s_waitcnt vmcnt(8)
	v_add_u32_e32 v18, v18, v7
	s_waitcnt vmcnt(7)
	v_add_u32_e32 v18, v18, v8
	s_waitcnt vmcnt(6)
	v_add_u32_e32 v18, v18, v9
	s_waitcnt vmcnt(5)
	v_add_u32_e32 v18, v18, v10
	s_waitcnt vmcnt(4)
	v_add_u32_e32 v18, v18, v11
	s_waitcnt vmcnt(3)
	v_add_u32_e32 v18, v18, v12
	s_waitcnt vmcnt(2)
	v_add_u32_e32 v18, v18, v13
	s_waitcnt vmcnt(1)
	v_add_u32_e32 v18, v18, v14
	s_waitcnt vmcnt(0)
	v_add_u32_e32 v18, v18, v15
	v_cmp_eq_u32_e32 vcc, s33, v18
	s_cbranch_vccnz .LBB0_2203
	s_and_b32 s42, s48, 0xff
	s_cmp_eq_u32 s42, 0
	s_mov_b64 s[42:43], -1
	s_mov_b64 s[46:47], -1
	s_sleep 4
	s_cbranch_scc0 .LBB0_2208
	global_load_dword v18, v17, s[4:5] sc1
	s_waitcnt vmcnt(0)
	v_cmp_eq_u32_e32 vcc, 0, v18
	s_cbranch_vccnz .LBB0_2210
	s_mov_b64 s[46:47], 0

.LBB0_2222:
	s_and_b32 s22, s26, 0xff
	s_mov_b64 s[18:19], -1
	s_cmp_lg_u32 s22, 0
	s_mov_b64 s[24:25], -1
	s_sleep 4
	s_cbranch_scc1 .LBB0_2225
	global_load_dword v3, v1, s[10:11] sc1
	s_waitcnt vmcnt(0)
	v_cmp_eq_u32_e32 vcc, 0, v3
	s_cbranch_vccnz .LBB0_2227
	s_mov_b64 s[24:25], 0
	s_mov_b64 s[22:23], -1

.LBB0_2239:
	s_and_b32 s18, s26, 0xff
	s_cmp_lg_u32 s18, 0
	s_mov_b64 s[22:23], -1
	s_sleep 4
	s_cbranch_scc1 .LBB0_2242
	global_load_dword v2, v1, s[10:11] sc1
	s_waitcnt vmcnt(0)
	v_cmp_eq_u32_e32 vcc, 0, v2
	s_cbranch_vccnz .LBB0_2244
	s_mov_b64 s[22:23], 0
	s_mov_b64 s[18:19], -1

.LBB0_2307:
	global_load_dword v16, v17, s[6:7] sc1
	global_load_dword v1, v17, s[8:9] sc1
	global_load_dword v2, v17, s[10:11] sc1
	global_load_dword v3, v17, s[12:13] sc1
	global_load_dword v4, v17, s[16:17] sc1
	global_load_dword v5, v17, s[18:19] sc1
	global_load_dword v6, v17, s[22:23] sc1
	global_load_dword v7, v17, s[24:25] sc1
	global_load_dword v8, v17, s[26:27] sc1
	global_load_dword v9, v17, s[28:29] sc1
	global_load_dword v10, v17, s[30:31] sc1
	global_load_dword v11, v17, s[34:35] sc1
	global_load_dword v12, v17, s[36:37] sc1
	global_load_dword v13, v17, s[38:39] sc1
	global_load_dword v14, v17, s[40:41] sc1
	global_load_dword v15, v17, s[42:43] sc1
	s_mov_b64 s[44:45], -1
	s_mov_b64 s[46:47], -1
	s_waitcnt vmcnt(14)
	v_add_u32_e32 v18, v1, v16
	s_waitcnt vmcnt(13)
	v_add_u32_e32 v18, v18, v2
	s_waitcnt vmcnt(12)
	v_add_u32_e32 v18, v18, v3
	s_waitcnt vmcnt(11)
	v_add_u32_e32 v18, v18, v4
	s_waitcnt vmcnt(10)
	v_add_u32_e32 v18, v18, v5
	s_waitcnt vmcnt(9)
	v_add_u32_e32 v18, v18, v6
	s_waitcnt vmcnt(8)
	v_add_u32_e32 v18, v18, v7
	s_waitcnt vmcnt(7)
	v_add_u32_e32 v18, v18, v8
	s_waitcnt vmcnt(6)
	v_add_u32_e32 v18, v18, v9
	s_waitcnt vmcnt(5)
	v_add_u32_e32 v18, v18, v10
	s_waitcnt vmcnt(4)
	v_add_u32_e32 v18, v18, v11
	s_waitcnt vmcnt(3)
	v_add_u32_e32 v18, v18, v12
	s_waitcnt vmcnt(2)
	v_add_u32_e32 v18, v18, v13
	s_waitcnt vmcnt(1)
	v_add_u32_e32 v18, v18, v14
	s_waitcnt vmcnt(0)
	v_add_u32_e32 v18, v18, v15
	v_cmp_eq_u32_e32 vcc, s51, v18
	s_cbranch_vccnz .LBB0_2306
	s_and_b32 s44, s58, 0xff
	s_cmp_eq_u32 s44, 0
	s_mov_b64 s[44:45], -1
	s_mov_b64 s[48:49], -1
	s_sleep 4
	s_cbranch_scc0 .LBB0_2311
	global_load_dword v18, v17, s[4:5] sc1
	s_waitcnt vmcnt(0)
	v_cmp_eq_u32_e32 vcc, 0, v18
	s_cbranch_vccnz .LBB0_2313
	s_mov_b64 s[48:49], 0

.LBB0_2325:
	s_and_b32 s24, s28, 0xff
	s_mov_b64 s[22:23], -1
	s_cmp_lg_u32 s24, 0
	s_mov_b64 s[26:27], -1
	s_sleep 4
	s_cbranch_scc1 .LBB0_2328
	global_load_dword v3, v1, s[10:11] sc1
	s_waitcnt vmcnt(0)
	v_cmp_eq_u32_e32 vcc, 0, v3
	s_cbranch_vccnz .LBB0_2330
	s_mov_b64 s[26:27], 0
	s_mov_b64 s[24:25], -1

.LBB0_2342:
	s_and_b32 s22, s28, 0xff
	s_cmp_lg_u32 s22, 0
	s_mov_b64 s[24:25], -1
	s_sleep 4
	s_cbranch_scc1 .LBB0_2345
	global_load_dword v2, v1, s[10:11] sc1
	s_waitcnt vmcnt(0)
	v_cmp_eq_u32_e32 vcc, 0, v2
	s_cbranch_vccnz .LBB0_2347
	s_mov_b64 s[24:25], 0
	s_mov_b64 s[22:23], -1

.LBB0_2378:
	global_load_dword v16, v17, s[8:9] sc1
	global_load_dword v1, v17, s[10:11] sc1
	global_load_dword v2, v17, s[12:13] sc1
	global_load_dword v3, v17, s[16:17] sc1
	global_load_dword v4, v17, s[18:19] sc1
	global_load_dword v5, v17, s[22:23] sc1
	global_load_dword v6, v17, s[24:25] sc1
	global_load_dword v7, v17, s[26:27] sc1
	global_load_dword v8, v17, s[28:29] sc1
	global_load_dword v9, v17, s[30:31] sc1
	global_load_dword v10, v17, s[34:35] sc1
	global_load_dword v11, v17, s[36:37] sc1
	global_load_dword v12, v17, s[38:39] sc1
	global_load_dword v13, v17, s[40:41] sc1
	global_load_dword v14, v17, s[42:43] sc1
	global_load_dword v15, v17, s[44:45] sc1
	s_mov_b64 s[46:47], -1
	s_mov_b64 s[48:49], -1
	s_waitcnt vmcnt(14)
	v_add_u32_e32 v18, v1, v16
	s_waitcnt vmcnt(13)
	v_add_u32_e32 v18, v18, v2
	s_waitcnt vmcnt(12)
	v_add_u32_e32 v18, v18, v3
	s_waitcnt vmcnt(11)
	v_add_u32_e32 v18, v18, v4
	s_waitcnt vmcnt(10)
	v_add_u32_e32 v18, v18, v5
	s_waitcnt vmcnt(9)
	v_add_u32_e32 v18, v18, v6
	s_waitcnt vmcnt(8)
	v_add_u32_e32 v18, v18, v7
	s_waitcnt vmcnt(7)
	v_add_u32_e32 v18, v18, v8
	s_waitcnt vmcnt(6)
	v_add_u32_e32 v18, v18, v9
	s_waitcnt vmcnt(5)
	v_add_u32_e32 v18, v18, v10
	s_waitcnt vmcnt(4)
	v_add_u32_e32 v18, v18, v11
	s_waitcnt vmcnt(3)
	v_add_u32_e32 v18, v18, v12
	s_waitcnt vmcnt(2)
	v_add_u32_e32 v18, v18, v13
	s_waitcnt vmcnt(1)
	v_add_u32_e32 v18, v18, v14
	s_waitcnt vmcnt(0)
	v_add_u32_e32 v18, v18, v15
	v_cmp_eq_u32_e32 vcc, s59, v18
	s_cbranch_vccnz .LBB0_2377
	s_and_b32 s46, s60, 0xff
	s_cmp_eq_u32 s46, 0
	s_mov_b64 s[46:47], -1
	s_mov_b64 s[50:51], -1
	s_sleep 4
	s_cbranch_scc0 .LBB0_2382
	global_load_dword v18, v17, s[6:7] sc1
	s_waitcnt vmcnt(0)
	v_cmp_eq_u32_e32 vcc, 0, v18
	s_cbranch_vccnz .LBB0_2384
	s_mov_b64 s[50:51], 0

.LBB0_2396:
	s_and_b32 s26, s30, 0xff
	s_mov_b64 s[24:25], -1
	s_cmp_lg_u32 s26, 0
	s_mov_b64 s[28:29], -1
	s_sleep 4
	s_cbranch_scc1 .LBB0_2399
	global_load_dword v3, v1, s[12:13] sc1
	s_waitcnt vmcnt(0)
	v_cmp_eq_u32_e32 vcc, 0, v3
	s_cbranch_vccnz .LBB0_2401
	s_mov_b64 s[28:29], 0
	s_mov_b64 s[26:27], -1

.LBB0_2413:
	s_and_b32 s24, s30, 0xff
	s_cmp_lg_u32 s24, 0
	s_mov_b64 s[26:27], -1
	s_sleep 4
	s_cbranch_scc1 .LBB0_2416
	global_load_dword v2, v1, s[12:13] sc1
	s_waitcnt vmcnt(0)
	v_cmp_eq_u32_e32 vcc, 0, v2
	s_cbranch_vccnz .LBB0_2418
	s_mov_b64 s[26:27], 0
	s_mov_b64 s[24:25], -1

.LBB0_2453:
	global_load_dword v15, v16, s[6:7] sc1
	global_load_dword v0, v16, s[8:9] sc1
	global_load_dword v1, v16, s[10:11] sc1
	global_load_dword v2, v16, s[12:13] sc1
	global_load_dword v3, v16, s[16:17] sc1
	global_load_dword v4, v16, s[18:19] sc1
	global_load_dword v5, v16, s[22:23] sc1
	global_load_dword v6, v16, s[24:25] sc1
	global_load_dword v7, v16, s[26:27] sc1
	global_load_dword v8, v16, s[28:29] sc1
	global_load_dword v9, v16, s[30:31] sc1
	global_load_dword v10, v16, s[34:35] sc1
	global_load_dword v11, v16, s[36:37] sc1
	global_load_dword v12, v16, s[38:39] sc1
	global_load_dword v13, v16, s[40:41] sc1
	global_load_dword v14, v16, s[42:43] sc1
	s_mov_b64 s[44:45], -1
	s_mov_b64 s[46:47], -1
	s_waitcnt vmcnt(14)
	v_add_u32_e32 v17, v0, v15
	s_waitcnt vmcnt(13)
	v_add_u32_e32 v17, v17, v1
	s_waitcnt vmcnt(12)
	v_add_u32_e32 v17, v17, v2
	s_waitcnt vmcnt(11)
	v_add_u32_e32 v17, v17, v3
	s_waitcnt vmcnt(10)
	v_add_u32_e32 v17, v17, v4
	s_waitcnt vmcnt(9)
	v_add_u32_e32 v17, v17, v5
	s_waitcnt vmcnt(8)
	v_add_u32_e32 v17, v17, v6
	s_waitcnt vmcnt(7)
	v_add_u32_e32 v17, v17, v7
	s_waitcnt vmcnt(6)
	v_add_u32_e32 v17, v17, v8
	s_waitcnt vmcnt(5)
	v_add_u32_e32 v17, v17, v9
	s_waitcnt vmcnt(4)
	v_add_u32_e32 v17, v17, v10
	s_waitcnt vmcnt(3)
	v_add_u32_e32 v17, v17, v11
	s_waitcnt vmcnt(2)
	v_add_u32_e32 v17, v17, v12
	s_waitcnt vmcnt(1)
	v_add_u32_e32 v17, v17, v13
	s_waitcnt vmcnt(0)
	v_add_u32_e32 v17, v17, v14
	v_cmp_eq_u32_e32 vcc, s33, v17
	s_cbranch_vccnz .LBB0_2452
	s_and_b32 s44, s50, 0xff
	s_cmp_eq_u32 s44, 0
	s_mov_b64 s[44:45], -1
	s_mov_b64 s[48:49], -1
	s_sleep 4
	s_cbranch_scc0 .LBB0_2457
	global_load_dword v17, v16, s[4:5] sc1
	s_waitcnt vmcnt(0)
	v_cmp_eq_u32_e32 vcc, 0, v17
	s_cbranch_vccnz .LBB0_2459
	s_mov_b64 s[48:49], 0

.LBB0_2471:
	s_and_b32 s24, s28, 0xff
	s_mov_b64 s[22:23], -1
	s_cmp_lg_u32 s24, 0
	s_mov_b64 s[26:27], -1
	s_sleep 4
	s_cbranch_scc1 .LBB0_2474
	global_load_dword v2, v0, s[10:11] sc1
	s_waitcnt vmcnt(0)
	v_cmp_eq_u32_e32 vcc, 0, v2
	s_cbranch_vccnz .LBB0_2476
	s_mov_b64 s[26:27], 0
	s_mov_b64 s[24:25], -1

.LBB0_2488:
	s_and_b32 s22, s28, 0xff
	s_cmp_lg_u32 s22, 0
	s_mov_b64 s[24:25], -1
	s_sleep 4
	s_cbranch_scc1 .LBB0_2491
	global_load_dword v1, v0, s[10:11] sc1
	s_waitcnt vmcnt(0)
	v_cmp_eq_u32_e32 vcc, 0, v1
	s_cbranch_vccnz .LBB0_2493
	s_mov_b64 s[24:25], 0
	s_mov_b64 s[22:23], -1
